# v83 + MoE GEMM phases: per-item expert lookup as one parallel compare+popcount instead of an 8-step LDS binary search
# speedup vs baseline: 1.0164x; 1.0164x over previous
.LBB0_777:
	s_add_i32 s44, s22, s3
	s_cmp_lt_i32 s44, s2
	s_cselect_b64 s[18:19], -1, 0
	s_cmp_ge_i32 s44, s2
	s_cselect_b64 s[0:1], -1, 0
	s_and_b64 vcc, exec, s[0:1]
	s_mov_b32 s8, s6
	s_mov_b32 s45, s7
	s_mov_b32 s46, s23
	v_mov_b32_e32 v176, v166
	s_waitcnt lgkmcnt(5)
	v_mov_b32_e32 v175, v139
	s_cbranch_vccnz .LBB0_781
	v_mbcnt_lo_u32_b32 v52, -1, 0
	v_mbcnt_hi_u32_b32 v52, -1, v52
	v_lshlrev_b32_e32 v52, 4, v52
	v_add_u32_e32 v52, 0x1f024, v52
	ds_read_b32 v53, v52
	ds_read_b32 v175, v52 offset:4
	ds_read_b32 v176, v52 offset:8
	ds_read_b32 v52, v52 offset:12
	s_ashr_i32 s9, s44, 2
	s_waitcnt lgkmcnt(0)
	v_cmp_ge_i32_e64 s[10:11], s9, v53
	v_cmp_ge_i32_e64 s[12:13], s9, v175
	s_bcnt1_i32_b64 s8, s[10:11]
	s_bcnt1_i32_b64 s10, s[12:13]
	s_add_i32 s8, s8, s10
	v_cmp_ge_i32_e64 s[10:11], s9, v176
	v_cmp_ge_i32_e64 s[12:13], s9, v52
	s_bcnt1_i32_b64 s10, s[10:11]
	s_bcnt1_i32_b64 s12, s[12:13]
	s_add_i32 s8, s8, s10
	s_add_i32 s8, s8, s12
	s_lshl_b32 s9, s8, 2
	s_add_i32 s9, s9, 0
	s_add_i32 s10, s9, 0x1f020
	v_mov_b32_e32 v52, s10
	ds_read2_b32 v[52:53], v52 offset1:1
	s_add_i32 s14, s9, 0x1e800
	s_add_i32 s9, s9, 0x1ec10
	s_waitcnt lgkmcnt(0)
	v_readfirstlane_b32 s10, v52
	v_mov_b32_e32 v52, s14
	ds_read_b32 v52, v52
	v_readfirstlane_b32 s11, v53
	s_sub_i32 s11, s11, s10
	s_lshl_b32 s10, s10, 2
	s_sub_i32 s10, s44, s10
	s_ashr_i32 s12, s10, 31
	v_mov_b32_e32 v53, s9
	s_lshr_b32 s12, s12, 30
	ds_read_b32 v175, v53
	s_waitcnt lgkmcnt(1)
	v_readfirstlane_b32 s9, v52
	s_add_i32 s12, s10, s12
	s_add_i32 s9, s9, s11
	s_ashr_i32 s13, s12, 2
	s_and_b32 s12, s12, -4
	s_add_i32 s9, s9, -1
	s_sub_i32 s45, s10, s12
	s_xor_b32 s10, s9, s11
	s_abs_i32 s11, s11
	v_cvt_f32_u32_e32 v53, s11
	s_sub_i32 s12, 0, s11
	s_abs_i32 s9, s9
	s_ashr_i32 s10, s10, 31
	v_rcp_iflag_f32_e32 v53, v53
	s_nop 0
	v_mul_f32_e32 v53, 0x4f7ffffe, v53
	v_cvt_u32_f32_e32 v53, v53
	s_nop 0
	v_readfirstlane_b32 s14, v53
	s_mul_i32 s12, s12, s14
	s_mul_hi_u32 s12, s14, s12
	s_add_i32 s14, s14, s12
	s_mul_hi_u32 s12, s9, s14
	s_mul_i32 s14, s12, s11
	s_sub_i32 s9, s9, s14
	s_add_i32 s14, s12, 1
	s_sub_i32 s15, s9, s11
	s_cmp_ge_u32 s9, s11
	s_cselect_b32 s12, s14, s12
	s_cselect_b32 s9, s15, s9
	s_add_i32 s14, s12, 1
	s_cmp_ge_u32 s9, s11
	s_cselect_b32 s9, s14, s12
	s_xor_b32 s9, s9, s10
	s_sub_i32 s9, s9, s10
	s_mul_i32 s46, s13, s9
	s_add_i32 s9, s46, s9
	v_min_i32_e32 v176, s9, v52

.LBB0_902:
	s_add_i32 s23, s12, s1
	s_cmp_lt_i32 s23, s0
	s_cselect_b64 s[4:5], -1, 0
	s_cmp_ge_i32 s23, s0
	s_cselect_b64 s[2:3], -1, 0
	s_and_b64 vcc, exec, s[2:3]
	s_mov_b32 s24, s13
	s_mov_b32 s25, s15
	s_mov_b32 s26, s14
	v_mov_b32_e32 v163, v156
	v_mov_b32_e32 v162, v141
	s_cbranch_vccnz .LBB0_906
	v_mbcnt_lo_u32_b32 v52, -1, 0
	v_mbcnt_hi_u32_b32 v52, -1, v52
	v_lshlrev_b32_e32 v52, 4, v52
	v_add_u32_e32 v52, 0x1f024, v52
	ds_read_b32 v53, v52
	ds_read_b32 v162, v52 offset:4
	ds_read_b32 v163, v52 offset:8
	ds_read_b32 v52, v52 offset:12
	s_ashr_i32 s6, s23, 3
	s_waitcnt lgkmcnt(0)
	v_cmp_ge_i32_e64 s[8:9], s6, v53
	v_cmp_ge_i32_e64 s[10:11], s6, v162
	s_bcnt1_i32_b64 s24, s[8:9]
	s_bcnt1_i32_b64 s8, s[10:11]
	s_add_i32 s24, s24, s8
	v_cmp_ge_i32_e64 s[8:9], s6, v163
	v_cmp_ge_i32_e64 s[10:11], s6, v52
	s_bcnt1_i32_b64 s8, s[8:9]
	s_bcnt1_i32_b64 s10, s[10:11]
	s_add_i32 s24, s24, s8
	s_add_i32 s24, s24, s10
	s_lshl_b32 s6, s24, 2
	s_add_i32 s6, s6, 0
	s_add_i32 s7, s6, 0x1f020
	v_mov_b32_e32 v52, s7
	ds_read2_b32 v[52:53], v52 offset1:1
	s_add_i32 s11, s6, 0x1e800
	s_add_i32 s6, s6, 0x1ec10
	s_waitcnt lgkmcnt(0)
	v_readfirstlane_b32 s7, v52
	v_mov_b32_e32 v52, s11
	ds_read_b32 v52, v52
	v_readfirstlane_b32 s8, v53
	s_sub_i32 s8, s8, s7
	s_lshl_b32 s7, s7, 3
	s_sub_i32 s7, s23, s7
	s_ashr_i32 s9, s7, 31
	v_mov_b32_e32 v53, s6
	s_lshr_b32 s9, s9, 29
	ds_read_b32 v162, v53
	s_waitcnt lgkmcnt(1)
	v_readfirstlane_b32 s6, v52
	s_add_i32 s9, s7, s9
	s_add_i32 s6, s6, s8
	s_ashr_i32 s10, s9, 3
	s_and_b32 s9, s9, -8
	s_add_i32 s6, s6, -1
	s_sub_i32 s25, s7, s9
	s_xor_b32 s7, s6, s8
	s_abs_i32 s8, s8
	v_cvt_f32_u32_e32 v53, s8
	s_sub_i32 s9, 0, s8
	s_abs_i32 s6, s6
	s_ashr_i32 s7, s7, 31
	v_rcp_iflag_f32_e32 v53, v53
	s_nop 0
	v_mul_f32_e32 v53, 0x4f7ffffe, v53
	v_cvt_u32_f32_e32 v53, v53
	s_nop 0
	v_readfirstlane_b32 s11, v53
	s_mul_i32 s9, s9, s11
	s_mul_hi_u32 s9, s11, s9
	s_add_i32 s11, s11, s9
	s_mul_hi_u32 s9, s6, s11
	s_mul_i32 s11, s9, s8
	s_sub_i32 s6, s6, s11
	s_add_i32 s11, s9, 1
	s_sub_i32 s26, s6, s8
	s_cmp_ge_u32 s6, s8
	s_cselect_b32 s9, s11, s9
	s_cselect_b32 s6, s26, s6
	s_add_i32 s11, s9, 1
	s_cmp_ge_u32 s6, s8
	s_cselect_b32 s6, s11, s9
	s_xor_b32 s6, s6, s7
	s_sub_i32 s6, s6, s7
	s_mul_i32 s26, s10, s6
	s_add_i32 s6, s26, s6
	v_min_i32_e32 v163, s6, v52

.LBB0_2357:
	s_add_i32 s47, s24, s3
	s_cmp_lt_i32 s47, s2
	s_cselect_b64 s[20:21], -1, 0
	s_cmp_ge_i32 s47, s2
	s_cselect_b64 s[8:9], -1, 0
	s_and_b64 vcc, exec, s[8:9]
	s_mov_b32 s10, s6
	s_mov_b32 s48, s7
	s_mov_b32 s49, s25
	v_mov_b32_e32 v176, v166
	s_waitcnt lgkmcnt(5)
	v_mov_b32_e32 v175, v139
	s_cbranch_vccnz .LBB0_2361
	v_mbcnt_lo_u32_b32 v52, -1, 0
	v_mbcnt_hi_u32_b32 v52, -1, v52
	v_lshlrev_b32_e32 v52, 4, v52
	v_add_u32_e32 v52, 0x1f024, v52
	ds_read_b32 v53, v52
	ds_read_b32 v54, v52 offset:4
	ds_read_b32 v55, v52 offset:8
	ds_read_b32 v52, v52 offset:12
	s_ashr_i32 s11, s47, 2
	s_waitcnt lgkmcnt(0)
	v_cmp_ge_i32_e64 s[12:13], s11, v53
	v_cmp_ge_i32_e64 s[14:15], s11, v54
	s_bcnt1_i32_b64 s10, s[12:13]
	s_bcnt1_i32_b64 s12, s[14:15]
	s_add_i32 s10, s10, s12
	v_cmp_ge_i32_e64 s[12:13], s11, v55
	v_cmp_ge_i32_e64 s[14:15], s11, v52
	s_bcnt1_i32_b64 s12, s[12:13]
	s_bcnt1_i32_b64 s14, s[14:15]
	s_add_i32 s10, s10, s12
	s_add_i32 s10, s10, s14
	s_lshl_b32 s11, s10, 2
	s_add_i32 s11, s11, 0
	s_add_i32 s12, s11, 0x1f020
	v_mov_b32_e32 v52, s12
	ds_read2_b32 v[52:53], v52 offset1:1
	s_add_i32 s12, s11, 0x1e800
	s_add_i32 s11, s11, 0x1ec10
	v_mov_b32_e32 v54, s12
	v_mov_b32_e32 v55, s11
	s_waitcnt lgkmcnt(0)
	v_readfirstlane_b32 s11, v52
	v_readfirstlane_b32 s12, v53
	s_sub_i32 s12, s12, s11
	s_abs_i32 s15, s12
	v_cvt_f32_u32_e32 v52, s15
	s_lshl_b32 s11, s11, 2
	s_sub_i32 s11, s47, s11
	ds_read_b32 v54, v54
	ds_read_b32 v175, v55
	v_rcp_iflag_f32_e32 v52, v52
	s_ashr_i32 s13, s11, 31
	s_lshr_b32 s13, s13, 30
	s_add_i32 s13, s11, s13
	v_mul_f32_e32 v52, 0x4f7ffffe, v52
	v_cvt_u32_f32_e32 v52, v52
	s_ashr_i32 s14, s13, 2
	s_and_b32 s13, s13, -4
	s_sub_i32 s48, s11, s13
	s_waitcnt lgkmcnt(1)
	v_readfirstlane_b32 s11, v54
	s_sub_i32 s13, 0, s15
	v_readfirstlane_b32 s16, v52
	s_add_i32 s11, s11, s12
	s_mul_i32 s13, s13, s16
	s_add_i32 s11, s11, -1
	s_mul_hi_u32 s13, s16, s13
	s_xor_b32 s12, s11, s12
	s_abs_i32 s11, s11
	s_add_i32 s16, s16, s13
	s_mul_hi_u32 s13, s11, s16
	s_mul_i32 s16, s13, s15
	s_sub_i32 s11, s11, s16
	s_ashr_i32 s12, s12, 31
	s_add_i32 s16, s13, 1
	s_sub_i32 s17, s11, s15
	s_cmp_ge_u32 s11, s15
	s_cselect_b32 s13, s16, s13
	s_cselect_b32 s11, s17, s11
	s_add_i32 s16, s13, 1
	s_cmp_ge_u32 s11, s15
	s_cselect_b32 s11, s16, s13
	s_xor_b32 s11, s11, s12
	s_sub_i32 s11, s11, s12
	s_mul_i32 s49, s14, s11
	s_add_i32 s11, s49, s11
	v_min_i32_e32 v176, s11, v54

.LBB0_2481:
	s_add_i32 s25, s12, s1
	s_cmp_lt_i32 s25, s0
	s_cselect_b64 s[4:5], -1, 0
	s_cmp_ge_i32 s25, s0
	s_cselect_b64 s[2:3], -1, 0
	s_and_b64 vcc, exec, s[2:3]
	s_mov_b32 s26, s13
	s_mov_b32 s27, s15
	s_mov_b32 s28, s14
	v_mov_b32_e32 v163, v156
	v_mov_b32_e32 v162, v141
	s_cbranch_vccnz .LBB0_2485
	v_mbcnt_lo_u32_b32 v52, -1, 0
	v_mbcnt_hi_u32_b32 v52, -1, v52
	v_lshlrev_b32_e32 v52, 4, v52
	v_add_u32_e32 v52, 0x1f024, v52
	ds_read_b32 v53, v52
	ds_read_b32 v54, v52 offset:4
	ds_read_b32 v55, v52 offset:8
	ds_read_b32 v52, v52 offset:12
	s_ashr_i32 s6, s25, 3
	s_waitcnt lgkmcnt(0)
	v_cmp_ge_i32_e64 s[8:9], s6, v53
	v_cmp_ge_i32_e64 s[10:11], s6, v54
	s_bcnt1_i32_b64 s26, s[8:9]
	s_bcnt1_i32_b64 s8, s[10:11]
	s_add_i32 s26, s26, s8
	v_cmp_ge_i32_e64 s[8:9], s6, v55
	v_cmp_ge_i32_e64 s[10:11], s6, v52
	s_bcnt1_i32_b64 s8, s[8:9]
	s_bcnt1_i32_b64 s10, s[10:11]
	s_add_i32 s26, s26, s8
	s_add_i32 s26, s26, s10
	s_lshl_b32 s6, s26, 2
	s_add_i32 s6, s6, 0
	s_add_i32 s7, s6, 0x1f020
	v_mov_b32_e32 v52, s7
	ds_read2_b32 v[52:53], v52 offset1:1
	s_add_i32 s7, s6, 0x1e800
	s_add_i32 s6, s6, 0x1ec10
	v_mov_b32_e32 v54, s7
	v_mov_b32_e32 v55, s6
	s_waitcnt lgkmcnt(0)
	v_readfirstlane_b32 s6, v52
	v_readfirstlane_b32 s7, v53
	s_sub_i32 s7, s7, s6
	s_abs_i32 s10, s7
	v_cvt_f32_u32_e32 v52, s10
	s_lshl_b32 s6, s6, 3
	s_sub_i32 s6, s25, s6
	ds_read_b32 v54, v54
	ds_read_b32 v162, v55
	v_rcp_iflag_f32_e32 v52, v52
	s_ashr_i32 s8, s6, 31
	s_lshr_b32 s8, s8, 29
	s_add_i32 s8, s6, s8
	v_mul_f32_e32 v52, 0x4f7ffffe, v52
	v_cvt_u32_f32_e32 v52, v52
	s_ashr_i32 s9, s8, 3
	s_and_b32 s8, s8, -8
	s_sub_i32 s27, s6, s8
	s_waitcnt lgkmcnt(1)
	v_readfirstlane_b32 s6, v54
	s_sub_i32 s8, 0, s10
	v_readfirstlane_b32 s11, v52
	s_add_i32 s6, s6, s7
	s_mul_i32 s8, s8, s11
	s_add_i32 s6, s6, -1
	s_mul_hi_u32 s8, s11, s8
	s_xor_b32 s7, s6, s7
	s_abs_i32 s6, s6
	s_add_i32 s11, s11, s8
	s_mul_hi_u32 s8, s6, s11
	s_mul_i32 s11, s8, s10
	s_sub_i32 s6, s6, s11
	s_ashr_i32 s7, s7, 31
	s_add_i32 s11, s8, 1
	s_sub_i32 s28, s6, s10
	s_cmp_ge_u32 s6, s10
	s_cselect_b32 s8, s11, s8
	s_cselect_b32 s6, s28, s6
	s_add_i32 s11, s8, 1
	s_cmp_ge_u32 s6, s10
	s_cselect_b32 s6, s11, s8
	s_xor_b32 s6, s6, s7
	s_sub_i32 s6, s6, s7
	s_mul_i32 s28, s9, s6
	s_add_i32 s6, s28, s6
	v_min_i32_e32 v163, s6, v54
